# phase 0: s_barrier between the trunk-conversion, fp8-conversion and row-normalisation sections keeps the 8 waves of a workgroup in step (homogeneous HBM traffic); on top of the 12-item conversion reba
# speedup vs baseline: 1.0314x; 1.0074x over previous
.LBB0_36:
	s_barrier
	s_mul_i32 s0, s38, 0xffffffa0
	s_add_i32 s0, s0, 0xd800
	s_cmp_gt_i32 s38, 64
	s_cselect_b32 s2, s0, 0xc000
	s_abs_i32 s0, s34
	v_cvt_f32_u32_e32 v1, s0
	s_sub_i32 s3, 0, s0
	s_add_i32 s1, s36, s34
	v_rcp_iflag_f32_e32 v1, v1
	s_nop 0
	v_mul_f32_e32 v1, 0x4f7ffffe, v1
	v_cvt_u32_f32_e32 v1, v1
	s_nop 0
	v_readfirstlane_b32 s4, v1
	s_mul_i32 s3, s3, s4
	s_mul_hi_u32 s3, s4, s3
	s_add_i32 s3, s4, s3
	s_mul_hi_u32 s4, s3, 0x690
	s_mul_i32 s4, s4, s0
	s_sub_i32 s4, 0x690, s4
	s_sub_i32 s5, s4, s0
	s_cmp_ge_u32 s4, s0
	s_cselect_b32 s4, s5, s4
	s_sub_i32 s5, s4, s0
	s_cmp_ge_u32 s4, s0
	s_cselect_b32 s4, s5, s4
	s_sub_i32 s1, s1, s4
	s_ashr_i32 s26, s1, 31
	s_abs_i32 s1, s1
	s_mul_hi_u32 s4, s1, s3
	s_mul_i32 s4, s4, s0
	s_sub_i32 s1, s1, s4
	s_sub_i32 s4, s1, s0
	s_cmp_ge_u32 s1, s0
	s_cselect_b32 s1, s4, s1
	s_sub_i32 s4, s1, s0
	s_cmp_ge_u32 s1, s0
	s_cselect_b32 s1, s4, s1
	s_xor_b32 s27, s1, s26
	s_sub_i32 s1, s27, s26
	s_cmp_gt_i32 s2, s1
	s_cbranch_scc0 .LBB0_38
	s_add_i32 s2, s34, s2
	s_not_b32 s5, s1
	s_add_i32 s5, s5, s2
	s_ashr_i32 s4, s34, 31
	s_ashr_i32 s2, s5, 31
	s_xor_b32 s2, s2, s4
	s_abs_i32 s4, s5
	s_mul_hi_u32 s3, s4, s3
	s_mul_i32 s5, s3, s0
	s_sub_i32 s4, s4, s5
	s_add_i32 s5, s3, 1
	s_sub_i32 s8, s4, s0
	s_cmp_ge_u32 s4, s0
	s_cselect_b32 s3, s5, s3
	s_cselect_b32 s4, s8, s4
	s_add_i32 s5, s3, 1
	s_cmp_ge_u32 s4, s0
	s_cselect_b32 s0, s5, s3
	s_xor_b32 s0, s0, s2
	s_sub_i32 s35, s0, s2

.LBB0_87:
	s_barrier
	s_cmpk_gt_i32 s36, 0x1fff
	v_and_b32_e32 v83, 64, v65
	v_xor_b32_e32 v81, 1, v65
	v_xor_b32_e32 v80, 2, v65
	v_xor_b32_e32 v79, 4, v65
	v_xor_b32_e32 v77, 8, v65
	v_xor_b32_e32 v75, 16, v65
	v_xor_b32_e32 v73, 32, v65
	s_cbranch_scc1 .LBB0_98
	v_add_u32_e32 v1, 64, v83
	s_load_dwordx2 s[0:1], s[22:23], 0x0
	v_cmp_lt_i32_e32 vcc, v81, v1
	s_lshl_b32 s4, s36, 2
	s_lshl_b32 s8, s38, 5
	v_cndmask_b32_e32 v2, v65, v81, vcc
	v_cmp_lt_i32_e32 vcc, v80, v1
	v_lshlrev_b32_e32 v84, 2, v2
	s_ashr_i32 s5, s4, 31
	v_cndmask_b32_e32 v2, v65, v80, vcc
	v_cmp_lt_i32_e32 vcc, v79, v1
	v_lshlrev_b32_e32 v85, 2, v2
	s_ashr_i32 s9, s8, 31
	v_cndmask_b32_e32 v2, v65, v79, vcc
	v_cmp_lt_i32_e32 vcc, v77, v1
	s_lshl_b64 s[14:15], s[4:5], 11
	v_lshlrev_b32_e32 v86, 2, v2
	v_cndmask_b32_e32 v2, v65, v77, vcc
	v_cmp_lt_i32_e32 vcc, v75, v1
	s_lshl_b64 s[10:11], s[4:5], 2
	s_lshl_b64 s[12:13], s[8:9], 2
	v_lshl_or_b32 v68, v0, 3, s14
	v_mov_b32_e32 v69, s15
	s_lshl_b64 s[14:15], s[8:9], 11
	s_lshl_b64 s[26:27], s[4:5], 12
	v_lshlrev_b32_e32 v87, 2, v2
	v_cndmask_b32_e32 v2, v65, v75, vcc
	v_cmp_lt_i32_e32 vcc, v73, v1
	s_waitcnt lgkmcnt(0)
	s_add_u32 s0, s0, s26
	v_mov_b32_e32 v67, 0
	v_cndmask_b32_e32 v1, v65, v73, vcc
	s_addc_u32 s1, s1, s27
	v_lshlrev_b32_e32 v89, 2, v1
	v_cmp_eq_u32_e64 s[2:3], 0, v0
	v_lshl_add_u64 v[0:1], s[0:1], 0, v[66:67]
	s_mov_b64 s[0:1], 0x3c00
	v_lshlrev_b32_e32 v88, 2, v2
	v_lshl_add_u64 v[70:71], v[0:1], 0, s[0:1]
	s_lshl_b64 s[26:27], s[8:9], 12
	v_mov_b32_e32 v67, 0x358637bd
	s_mov_b32 s0, 0x800000
	v_mov_b32_e32 v90, 0x380000
	s_mov_b32 s1, 0x12400000
	s_mov_b32 s5, 0x12401000
	s_branch .LBB0_90
